# v56: v51 with s_sleep removed from grid-barrier and queue spin loops (tight polling)
# baseline (speedup 1.0000x reference)
.LBB0_18:
	v_readlane_b32 s14, v253, 3
	v_readlane_b32 s15, v253, 4
	s_nop 4
	global_load_dword v11, v17, s[14:15] offset:1024 sc1
	global_load_dword v1, v17, s[14:15] offset:1280 sc1
	global_load_dword v2, v17, s[14:15] offset:1536 sc1
	global_load_dword v3, v17, s[14:15] offset:1792 sc1
	global_load_dword v4, v17, s[14:15] offset:2048 sc1
	global_load_dword v5, v17, s[14:15] offset:2304 sc1
	global_load_dword v6, v17, s[14:15] offset:2560 sc1
	global_load_dword v7, v17, s[14:15] offset:2816 sc1
	global_load_dword v8, v17, s[14:15] offset:3072 sc1
	global_load_dword v9, v17, s[14:15] offset:3328 sc1
	global_load_dword v10, v17, s[14:15] offset:3584 sc1
	global_load_dword v12, v17, s[14:15] offset:3840 sc1
	global_load_dword v13, v17, s[4:5] sc1
	global_load_dword v14, v17, s[8:9] sc1
	global_load_dword v15, v17, s[10:11] sc1
	global_load_dword v16, v17, s[12:13] sc1
	s_mov_b64 s[14:15], -1
	s_mov_b64 s[16:17], -1
	s_waitcnt vmcnt(14)
	v_add_u32_e32 v18, v1, v11
	s_waitcnt vmcnt(13)
	v_add_u32_e32 v18, v18, v2
	s_waitcnt vmcnt(12)
	v_add_u32_e32 v18, v18, v3
	s_waitcnt vmcnt(11)
	v_add_u32_e32 v18, v18, v4
	s_waitcnt vmcnt(10)
	v_add_u32_e32 v18, v18, v5
	s_waitcnt vmcnt(9)
	v_add_u32_e32 v18, v18, v6
	s_waitcnt vmcnt(8)
	v_add_u32_e32 v18, v18, v7
	s_waitcnt vmcnt(7)
	v_add_u32_e32 v18, v18, v8
	s_waitcnt vmcnt(6)
	v_add_u32_e32 v18, v18, v9
	s_waitcnt vmcnt(5)
	v_add_u32_e32 v18, v18, v10
	s_waitcnt vmcnt(4)
	v_add_u32_e32 v18, v18, v12
	s_waitcnt vmcnt(3)
	v_add_u32_e32 v18, v18, v13
	s_waitcnt vmcnt(2)
	v_add_u32_e32 v18, v18, v14
	s_waitcnt vmcnt(1)
	v_add_u32_e32 v18, v18, v15
	s_waitcnt vmcnt(0)
	v_add_u32_e32 v18, v18, v16
	v_cmp_eq_u32_e32 vcc, s20, v18
	s_cbranch_vccnz .LBB0_17
	s_and_b32 s14, s21, 0xff
	s_cmp_eq_u32 s14, 0
	s_mov_b64 s[14:15], -1
	s_mov_b64 s[18:19], -1
	s_cbranch_scc1 .LBB0_22
	s_and_b64 vcc, exec, s[18:19]
	s_cbranch_vccz .LBB0_17

.LBB0_95:
	s_and_b32 s22, s28, 0xff
	s_cmp_lg_u32 s22, 0
	s_mov_b64 s[24:25], -1
	s_cbranch_scc0 .LBB0_98
	s_mov_b64 s[26:27], -1
	s_and_b64 vcc, exec, s[24:25]
	s_cbranch_vccz .LBB0_94

.LBB0_231:
	s_and_b32 s12, s16, 0xff
	s_mov_b64 s[10:11], -1
	s_cmp_lg_u32 s12, 0
	s_mov_b64 s[14:15], -1
	s_cbranch_scc0 .LBB0_234
	s_and_b64 vcc, exec, s[14:15]
	s_cbranch_vccz .LBB0_230

.LBB0_331:
	v_readlane_b32 s2, v253, 3
	v_readlane_b32 s3, v253, 4
	s_nop 4
	global_load_dword v13, v3, s[2:3] offset:1024 sc1
	global_load_dword v2, v3, s[2:3] offset:1280 sc1
	global_load_dword v4, v3, s[2:3] offset:1536 sc1
	global_load_dword v5, v3, s[2:3] offset:1792 sc1
	global_load_dword v6, v3, s[2:3] offset:2048 sc1
	global_load_dword v7, v3, s[2:3] offset:2304 sc1
	global_load_dword v8, v3, s[2:3] offset:2560 sc1
	global_load_dword v9, v3, s[2:3] offset:2816 sc1
	global_load_dword v10, v3, s[2:3] offset:3072 sc1
	global_load_dword v11, v3, s[2:3] offset:3328 sc1
	global_load_dword v12, v3, s[2:3] offset:3584 sc1
	global_load_dword v14, v3, s[2:3] offset:3840 sc1
	v_readlane_b32 s2, v253, 7
	v_readlane_b32 s3, v253, 8
	s_mov_b64 s[4:5], -1
	s_waitcnt vmcnt(10)
	v_add_u32_e32 v19, v2, v13
	s_nop 1
	global_load_dword v15, v3, s[2:3] sc1
	v_readlane_b32 s2, v253, 9
	v_readlane_b32 s3, v253, 10
	s_waitcnt vmcnt(10)
	v_add_u32_e32 v19, v19, v4
	s_waitcnt vmcnt(9)
	v_add_u32_e32 v19, v19, v5
	s_waitcnt vmcnt(8)
	v_add_u32_e32 v19, v19, v6
	s_waitcnt vmcnt(7)
	v_add_u32_e32 v19, v19, v7
	s_waitcnt vmcnt(6)
	v_add_u32_e32 v19, v19, v8
	global_load_dword v16, v3, s[2:3] sc1
	v_readlane_b32 s2, v253, 11
	v_readlane_b32 s3, v253, 12
	s_waitcnt vmcnt(6)
	v_add_u32_e32 v19, v19, v9
	s_waitcnt vmcnt(5)
	v_add_u32_e32 v19, v19, v10
	s_waitcnt vmcnt(4)
	v_add_u32_e32 v19, v19, v11
	s_waitcnt vmcnt(3)
	v_add_u32_e32 v19, v19, v12
	s_waitcnt vmcnt(2)
	v_add_u32_e32 v19, v19, v14
	global_load_dword v17, v3, s[2:3] sc1
	v_readlane_b32 s2, v253, 13
	v_readlane_b32 s3, v253, 14
	s_waitcnt vmcnt(2)
	v_add_u32_e32 v19, v19, v15
	s_nop 2
	global_load_dword v18, v3, s[2:3] sc1
	s_mov_b64 s[2:3], -1
	s_waitcnt vmcnt(2)
	v_add_u32_e32 v19, v19, v16
	s_waitcnt vmcnt(1)
	v_add_u32_e32 v19, v19, v17
	s_waitcnt vmcnt(0)
	v_add_u32_e32 v19, v19, v18
	v_cmp_eq_u32_e32 vcc, s10, v19
	s_cbranch_vccnz .LBB0_330
	s_and_b32 s2, s11, 0xff
	s_cmp_eq_u32 s2, 0
	s_mov_b64 s[2:3], -1
	s_mov_b64 s[8:9], -1
	s_cbranch_scc1 .LBB0_335
	s_and_b64 vcc, exec, s[8:9]
	s_cbranch_vccz .LBB0_330

.LBB0_362:
	s_and_b32 s16, s20, 0xff
	s_mov_b64 s[14:15], -1
	s_cmp_lg_u32 s16, 0
	s_mov_b64 s[18:19], -1
	s_cbranch_scc0 .LBB0_365
	s_and_b64 vcc, exec, s[18:19]
	s_cbranch_vccz .LBB0_361

.LBB0_391:
	s_and_b32 s10, s14, 0xff
	s_mov_b64 s[8:9], -1
	s_cmp_lg_u32 s10, 0
	s_mov_b64 s[12:13], -1
	s_cbranch_scc0 .LBB0_394
	s_and_b64 vcc, exec, s[12:13]
	s_cbranch_vccz .LBB0_390

.LBB0_562:
	v_readlane_b32 s0, v253, 3
	v_readlane_b32 s1, v253, 4
	s_nop 4
	global_load_dword v13, v3, s[0:1] offset:1024 sc1
	global_load_dword v2, v3, s[0:1] offset:1280 sc1
	global_load_dword v4, v3, s[0:1] offset:1536 sc1
	global_load_dword v5, v3, s[0:1] offset:1792 sc1
	global_load_dword v6, v3, s[0:1] offset:2048 sc1
	global_load_dword v7, v3, s[0:1] offset:2304 sc1
	global_load_dword v8, v3, s[0:1] offset:2560 sc1
	global_load_dword v9, v3, s[0:1] offset:2816 sc1
	global_load_dword v10, v3, s[0:1] offset:3072 sc1
	global_load_dword v11, v3, s[0:1] offset:3328 sc1
	global_load_dword v12, v3, s[0:1] offset:3584 sc1
	global_load_dword v14, v3, s[0:1] offset:3840 sc1
	v_readlane_b32 s0, v253, 7
	v_readlane_b32 s1, v253, 8
	s_mov_b64 s[2:3], -1
	s_waitcnt vmcnt(10)
	v_add_u32_e32 v19, v2, v13
	s_nop 1
	global_load_dword v15, v3, s[0:1] sc1
	v_readlane_b32 s0, v253, 9
	v_readlane_b32 s1, v253, 10
	s_waitcnt vmcnt(10)
	v_add_u32_e32 v19, v19, v4
	s_waitcnt vmcnt(9)
	v_add_u32_e32 v19, v19, v5
	s_waitcnt vmcnt(8)
	v_add_u32_e32 v19, v19, v6
	s_waitcnt vmcnt(7)
	v_add_u32_e32 v19, v19, v7
	s_waitcnt vmcnt(6)
	v_add_u32_e32 v19, v19, v8
	global_load_dword v16, v3, s[0:1] sc1
	v_readlane_b32 s0, v253, 11
	v_readlane_b32 s1, v253, 12
	s_waitcnt vmcnt(6)
	v_add_u32_e32 v19, v19, v9
	s_waitcnt vmcnt(5)
	v_add_u32_e32 v19, v19, v10
	s_waitcnt vmcnt(4)
	v_add_u32_e32 v19, v19, v11
	s_waitcnt vmcnt(3)
	v_add_u32_e32 v19, v19, v12
	s_waitcnt vmcnt(2)
	v_add_u32_e32 v19, v19, v14
	global_load_dword v17, v3, s[0:1] sc1
	v_readlane_b32 s0, v253, 13
	v_readlane_b32 s1, v253, 14
	s_waitcnt vmcnt(2)
	v_add_u32_e32 v19, v19, v15
	s_nop 2
	global_load_dword v18, v3, s[0:1] sc1
	s_mov_b64 s[0:1], -1
	s_waitcnt vmcnt(2)
	v_add_u32_e32 v19, v19, v16
	s_waitcnt vmcnt(1)
	v_add_u32_e32 v19, v19, v17
	s_waitcnt vmcnt(0)
	v_add_u32_e32 v19, v19, v18
	v_cmp_eq_u32_e32 vcc, s10, v19
	s_cbranch_vccnz .LBB0_561
	s_and_b32 s0, s11, 0xff
	s_cmp_eq_u32 s0, 0
	s_mov_b64 s[0:1], -1
	s_mov_b64 s[8:9], -1
	s_cbranch_scc1 .LBB0_566
	s_and_b64 vcc, exec, s[8:9]
	s_cbranch_vccz .LBB0_561

.LBB0_823:
	v_readlane_b32 s0, v253, 3
	v_readlane_b32 s1, v253, 4
	s_nop 4
	global_load_dword v13, v3, s[0:1] offset:1024 sc1
	global_load_dword v2, v3, s[0:1] offset:1280 sc1
	global_load_dword v4, v3, s[0:1] offset:1536 sc1
	global_load_dword v5, v3, s[0:1] offset:1792 sc1
	global_load_dword v6, v3, s[0:1] offset:2048 sc1
	global_load_dword v7, v3, s[0:1] offset:2304 sc1
	global_load_dword v8, v3, s[0:1] offset:2560 sc1
	global_load_dword v9, v3, s[0:1] offset:2816 sc1
	global_load_dword v10, v3, s[0:1] offset:3072 sc1
	global_load_dword v11, v3, s[0:1] offset:3328 sc1
	global_load_dword v12, v3, s[0:1] offset:3584 sc1
	global_load_dword v14, v3, s[0:1] offset:3840 sc1
	v_readlane_b32 s0, v253, 7
	v_readlane_b32 s1, v253, 8
	s_mov_b64 s[2:3], -1
	s_waitcnt vmcnt(10)
	v_add_u32_e32 v19, v2, v13
	s_nop 1
	global_load_dword v15, v3, s[0:1] sc1
	v_readlane_b32 s0, v253, 9
	v_readlane_b32 s1, v253, 10
	s_waitcnt vmcnt(10)
	v_add_u32_e32 v19, v19, v4
	s_waitcnt vmcnt(9)
	v_add_u32_e32 v19, v19, v5
	s_waitcnt vmcnt(8)
	v_add_u32_e32 v19, v19, v6
	s_waitcnt vmcnt(7)
	v_add_u32_e32 v19, v19, v7
	s_waitcnt vmcnt(6)
	v_add_u32_e32 v19, v19, v8
	global_load_dword v16, v3, s[0:1] sc1
	v_readlane_b32 s0, v253, 11
	v_readlane_b32 s1, v253, 12
	s_waitcnt vmcnt(6)
	v_add_u32_e32 v19, v19, v9
	s_waitcnt vmcnt(5)
	v_add_u32_e32 v19, v19, v10
	s_waitcnt vmcnt(4)
	v_add_u32_e32 v19, v19, v11
	s_waitcnt vmcnt(3)
	v_add_u32_e32 v19, v19, v12
	s_waitcnt vmcnt(2)
	v_add_u32_e32 v19, v19, v14
	global_load_dword v17, v3, s[0:1] sc1
	v_readlane_b32 s0, v253, 13
	v_readlane_b32 s1, v253, 14
	s_waitcnt vmcnt(2)
	v_add_u32_e32 v19, v19, v15
	s_nop 2
	global_load_dword v18, v3, s[0:1] sc1
	s_mov_b64 s[0:1], -1
	s_waitcnt vmcnt(2)
	v_add_u32_e32 v19, v19, v16
	s_waitcnt vmcnt(1)
	v_add_u32_e32 v19, v19, v17
	s_waitcnt vmcnt(0)
	v_add_u32_e32 v19, v19, v18
	v_cmp_eq_u32_e32 vcc, s8, v19
	s_cbranch_vccnz .LBB0_822
	s_and_b32 s0, s9, 0xff
	s_cmp_eq_u32 s0, 0
	s_mov_b64 s[0:1], -1
	s_mov_b64 s[4:5], -1
	s_cbranch_scc1 .LBB0_827
	s_and_b64 vcc, exec, s[4:5]
	s_cbranch_vccz .LBB0_822

.LBB0_854:
	s_and_b32 s14, s18, 0xff
	s_mov_b64 s[12:13], -1
	s_cmp_lg_u32 s14, 0
	s_mov_b64 s[16:17], -1
	s_cbranch_scc0 .LBB0_857
	s_and_b64 vcc, exec, s[16:17]
	s_cbranch_vccz .LBB0_853

.LBB0_1150:
	s_and_b32 s18, s22, 0xff
	s_mov_b64 s[16:17], -1
	s_cmp_lg_u32 s18, 0
	s_mov_b64 s[20:21], -1
	s_cbranch_scc0 .LBB0_1153
	s_and_b64 vcc, exec, s[20:21]
	s_cbranch_vccz .LBB0_1149

.LBB0_1565:
	v_readlane_b32 s2, v253, 3
	v_readlane_b32 s3, v253, 4
	s_nop 4
	global_load_dword v13, v3, s[2:3] offset:1024 sc1
	global_load_dword v2, v3, s[2:3] offset:1280 sc1
	global_load_dword v4, v3, s[2:3] offset:1536 sc1
	global_load_dword v5, v3, s[2:3] offset:1792 sc1
	global_load_dword v6, v3, s[2:3] offset:2048 sc1
	global_load_dword v7, v3, s[2:3] offset:2304 sc1
	global_load_dword v8, v3, s[2:3] offset:2560 sc1
	global_load_dword v9, v3, s[2:3] offset:2816 sc1
	global_load_dword v10, v3, s[2:3] offset:3072 sc1
	global_load_dword v11, v3, s[2:3] offset:3328 sc1
	global_load_dword v12, v3, s[2:3] offset:3584 sc1
	global_load_dword v14, v3, s[2:3] offset:3840 sc1
	v_readlane_b32 s2, v253, 7
	v_readlane_b32 s3, v253, 8
	s_mov_b64 s[4:5], -1
	s_waitcnt vmcnt(10)
	v_add_u32_e32 v19, v2, v13
	s_nop 1
	global_load_dword v15, v3, s[2:3] sc1
	v_readlane_b32 s2, v253, 9
	v_readlane_b32 s3, v253, 10
	s_waitcnt vmcnt(10)
	v_add_u32_e32 v19, v19, v4
	s_waitcnt vmcnt(9)
	v_add_u32_e32 v19, v19, v5
	s_waitcnt vmcnt(8)
	v_add_u32_e32 v19, v19, v6
	s_waitcnt vmcnt(7)
	v_add_u32_e32 v19, v19, v7
	s_waitcnt vmcnt(6)
	v_add_u32_e32 v19, v19, v8
	global_load_dword v16, v3, s[2:3] sc1
	v_readlane_b32 s2, v253, 11
	v_readlane_b32 s3, v253, 12
	s_waitcnt vmcnt(6)
	v_add_u32_e32 v19, v19, v9
	s_waitcnt vmcnt(5)
	v_add_u32_e32 v19, v19, v10
	s_waitcnt vmcnt(4)
	v_add_u32_e32 v19, v19, v11
	s_waitcnt vmcnt(3)
	v_add_u32_e32 v19, v19, v12
	s_waitcnt vmcnt(2)
	v_add_u32_e32 v19, v19, v14
	global_load_dword v17, v3, s[2:3] sc1
	v_readlane_b32 s2, v253, 13
	v_readlane_b32 s3, v253, 14
	s_waitcnt vmcnt(2)
	v_add_u32_e32 v19, v19, v15
	s_nop 2
	global_load_dword v18, v3, s[2:3] sc1
	s_mov_b64 s[2:3], -1
	s_waitcnt vmcnt(2)
	v_add_u32_e32 v19, v19, v16
	s_waitcnt vmcnt(1)
	v_add_u32_e32 v19, v19, v17
	s_waitcnt vmcnt(0)
	v_add_u32_e32 v19, v19, v18
	v_cmp_eq_u32_e32 vcc, s12, v19
	s_cbranch_vccnz .LBB0_1564
	s_and_b32 s2, s13, 0xff
	s_cmp_eq_u32 s2, 0
	s_mov_b64 s[2:3], -1
	s_mov_b64 s[10:11], -1
	s_cbranch_scc1 .LBB0_1569
	s_and_b64 vcc, exec, s[10:11]
	s_cbranch_vccz .LBB0_1564
